# c42: c41 + prologue memory-rows loop: the four norm-gain row pieces are loaded up front instead of load-wait one at a time
# baseline (speedup 1.0000x reference)
; __device__ __forceinline__ unsigned pk4_fp8(float a, float b, float c, float d) { int w = 0; w = __builtin_amdgcn_cvt_pk_fp8_f32(a, b, w, false); w = __builtin_amdgcn_cvt_pk_fp8_f32(c, d, w, true); return (unsigned)w; }
; #define GAS __attribute__((address_space(1)))
; __device__ __forceinline__ void rms_row_f8(const float* xrow, const float* gain, unsigned char* o8b, int lane) {
;     const GAS f32x4* xr = (const GAS f32x4*)xrow + lane; const GAS f32x4* gr = (const GAS f32x4*)gain + lane;
;     f32x4 v[4]; float s = 0.f;
; #pragma unroll
;     for (int j = 0; j < 4; ++j) { v[j] = xr[64 * j]; s += (v[j].x * v[j].x + v[j].y * v[j].y) + (v[j].z * v[j].z + v[j].w * v[j].w); }
;     const float rstd = 1.0f / sqrtf(wave_sum(s) * (1.0f / DM) + RMS_EPS);
; #pragma unroll
;     for (int j = 0; j < 4; ++j) { const f32x4 g = gr[64 * j]; const f32x4 y = v[j] * rstd * g; ((GAS unsigned*)o8b)[lane + 64 * j] = pg8::pk4_fp8(y.x, y.y, y.z, y.w); }
; }
.LBB0_75:
	global_load_dwordx4 v[16:19], v[6:7], off offset:-3072
	global_load_dwordx4 v[20:23], v[6:7], off offset:-2048
	global_load_dwordx4 v[24:27], v[6:7], off offset:-1024
	global_load_dwordx4 v[28:31], v[6:7], off
	global_load_dwordx4 v[32:35], v[2:3], off
	global_load_dwordx4 v[100:103], v[2:3], off offset:1024
	global_load_dwordx4 v[104:107], v[2:3], off offset:2048
	global_load_dwordx4 v[108:111], v[2:3], off offset:3072
	v_mov_b32_e32 v47, 0
	s_addk_i32 s3, 0x800
	v_lshl_add_u64 v[6:7], v[6:7], 0, s[14:15]
	s_cmpk_gt_i32 s3, 0xf8ff
	s_waitcnt vmcnt(7)
	v_pk_mul_f32 v[36:37], v[18:19], v[18:19]
	v_pk_mul_f32 v[38:39], v[16:17], v[16:17]
	s_waitcnt vmcnt(6)
	v_pk_mul_f32 v[40:41], v[22:23], v[22:23]
	v_pk_mul_f32 v[42:43], v[20:21], v[20:21]
	v_pk_mov_b32 v[48:49], v[38:39], v[36:37] op_sel:[1,0]
	v_mov_b32_e32 v39, v37
	v_pk_mov_b32 v[36:37], v[42:43], v[40:41] op_sel:[1,0]
	v_mov_b32_e32 v43, v41
	s_waitcnt vmcnt(5)
	v_mul_f32_e32 v44, v25, v25
	v_mul_f32_e32 v46, v27, v27
	v_pk_add_f32 v[38:39], v[48:49], v[38:39]
	v_pk_add_f32 v[36:37], v[36:37], v[42:43]
	s_waitcnt vmcnt(4)
	v_mul_f32_e32 v50, v28, v28
	v_mul_f32_e32 v51, v29, v29
	v_mul_f32_e32 v52, v30, v30
	v_mul_f32_e32 v53, v31, v31
	v_pk_fma_f32 v[40:41], v[24:25], v[24:25], v[44:45] op_sel_hi:[1,1,0]
	v_pk_fma_f32 v[44:45], v[26:27], v[26:27], v[46:47] op_sel_hi:[1,1,0]
	v_pk_add_f32 v[38:39], v[38:39], v[38:39] op_sel:[0,1] op_sel_hi:[1,0]
	v_pk_add_f32 v[36:37], v[36:37], v[36:37] op_sel:[0,1] op_sel_hi:[1,0]
	v_mov_b32_e32 v41, v52
	v_mov_b32_e32 v45, v53
	v_mov_b32_e32 v39, v50
	v_mov_b32_e32 v37, v51
	v_pk_add_f32 v[40:41], v[40:41], v[44:45]
	v_pk_add_f32 v[36:37], v[38:39], v[36:37]
	s_nop 0
	v_pk_add_f32 v[36:37], v[36:37], v[40:41]
	s_nop 0
	v_add_f32_e32 v36, v36, v37
	ds_bpermute_b32 v37, v8, v36
	s_waitcnt lgkmcnt(0)
	v_add_f32_e32 v36, v36, v37
	ds_bpermute_b32 v37, v9, v36
	s_waitcnt lgkmcnt(0)
	v_add_f32_e32 v36, v36, v37
	ds_bpermute_b32 v37, v10, v36
	s_waitcnt lgkmcnt(0)
	v_add_f32_e32 v36, v36, v37
	ds_bpermute_b32 v37, v11, v36
	s_waitcnt lgkmcnt(0)
	v_add_f32_e32 v36, v36, v37
	ds_bpermute_b32 v37, v12, v36
	s_waitcnt lgkmcnt(0)
	v_add_f32_e32 v36, v36, v37
	ds_bpermute_b32 v37, v13, v36
	s_waitcnt lgkmcnt(0)
	v_add_f32_e32 v36, v36, v37
	v_fmamk_f32 v36, v36, 0x3a800000, v14
	v_mul_f32_e32 v37, 0x4f800000, v36
	v_cmp_gt_f32_e32 vcc, s4, v36
	s_nop 1
	v_cndmask_b32_e32 v36, v36, v37, vcc
	v_sqrt_f32_e32 v37, v36
	s_nop 0
	v_add_u32_e32 v38, -1, v37
	v_add_u32_e32 v39, 1, v37
	v_fma_f32 v40, -v38, v37, v36
	v_fma_f32 v41, -v39, v37, v36
	v_cmp_ge_f32_e64 s[8:9], 0, v40
	s_nop 1
	v_cndmask_b32_e64 v37, v37, v38, s[8:9]
	v_cmp_lt_f32_e64 s[8:9], 0, v41
	s_nop 1
	v_cndmask_b32_e64 v37, v37, v39, s[8:9]
	v_mul_f32_e32 v38, 0x37800000, v37
	v_cndmask_b32_e32 v37, v37, v38, vcc
	v_cmp_class_f32_e32 vcc, v36, v15
	s_nop 1
	v_cndmask_b32_e32 v36, v37, v36, vcc
	v_div_scale_f32 v37, s[6:7], v36, v36, 1.0
	v_rcp_f32_e32 v38, v37
	v_div_scale_f32 v39, vcc, 1.0, v36, 1.0
	v_fma_f32 v40, -v37, v38, 1.0
	v_fmac_f32_e32 v38, v40, v38
	v_mul_f32_e32 v40, v39, v38
	v_fma_f32 v41, -v37, v40, v39
	v_fmac_f32_e32 v40, v41, v38
	v_fma_f32 v37, -v37, v40, v39
	v_div_fmas_f32 v37, v37, v38, v40
	v_div_fixup_f32 v36, v37, v36, 1.0
	v_pk_mul_f32 v[16:17], v[16:17], v[36:37] op_sel_hi:[1,0]
	v_pk_mul_f32 v[20:21], v[20:21], v[36:37] op_sel_hi:[1,0]
	s_waitcnt vmcnt(3)
	v_pk_mul_f32 v[16:17], v[32:33], v[16:17]
	v_mov_b32_e32 v32, 0
	v_cvt_pk_fp8_f32 v47, v16, v17
	v_pk_mul_f32 v[16:17], v[18:19], v[36:37] op_sel_hi:[1,0]
	s_nop 0
	v_pk_mul_f32 v[16:17], v[34:35], v[16:17]
	s_nop 0
	v_cvt_pk_fp8_f32 v47, v16, v17 op_sel:[0,0,1]
	global_store_dword v[4:5], v47, off
	s_waitcnt vmcnt(3)
	v_pk_mul_f32 v[16:17], v[100:101], v[20:21]
	s_nop 0
	v_cvt_pk_fp8_f32 v32, v16, v17
	v_pk_mul_f32 v[16:17], v[22:23], v[36:37] op_sel_hi:[1,0]
	v_pk_mul_f32 v[20:21], v[24:25], v[36:37] op_sel_hi:[1,0]
	v_pk_mul_f32 v[16:17], v[102:103], v[16:17]
	v_mov_b32_e32 v22, 0
	v_cvt_pk_fp8_f32 v32, v16, v17 op_sel:[0,0,1]
	global_store_dword v[4:5], v32, off offset:256
	s_waitcnt vmcnt(3)
	v_pk_mul_f32 v[16:17], v[104:105], v[20:21]
	s_nop 0
	v_cvt_pk_fp8_f32 v22, v16, v17
	v_pk_mul_f32 v[16:17], v[26:27], v[36:37] op_sel_hi:[1,0]
	v_pk_mul_f32 v[20:21], v[28:29], v[36:37] op_sel_hi:[1,0]
	v_pk_mul_f32 v[16:17], v[106:107], v[16:17]
	s_nop 0
	v_cvt_pk_fp8_f32 v22, v16, v17 op_sel:[0,0,1]
	global_store_dword v[4:5], v22, off offset:512
	v_mov_b32_e32 v22, 0
	s_waitcnt vmcnt(3)
	v_pk_mul_f32 v[16:17], v[20:21], v[108:109]
	s_nop 0
	v_cvt_pk_fp8_f32 v22, v16, v17
	v_pk_mul_f32 v[16:17], v[30:31], v[36:37] op_sel_hi:[1,0]
	s_nop 0
	v_pk_mul_f32 v[16:17], v[16:17], v[110:111]
	s_nop 0
	v_cvt_pk_fp8_f32 v22, v16, v17 op_sel:[0,0,1]
	global_store_dword v[4:5], v22, off offset:768
	v_lshl_add_u64 v[4:5], v[4:5], 0, s[12:13]
	s_cbranch_scc0 .LBB0_75
